# P11 unit traversal per XCD: 4 row tiles x 8 column tiles per round (each activation panel re-read in 2 rounds instead of 4, same L2 fill traffic)
# speedup vs baseline: 1.0135x; 1.0135x over previous
; #define PG8_STAGE(bufoff, gbase, voff) do { const char* _gb = (const char*)(gbase); asm volatile("" : "+s"(_gb)); _Pragma("unroll") for (int _i = 0; _i < 2; ++_i) \
;         __builtin_amdgcn_global_load_lds((const unsigned*)(_gb + (voff)[_i]), (PG8_LAS unsigned*)(lds + (bufoff) + ldsw + _i * 8192), 16, 0, 0); } while (0)
; #define PG8_WAIT_V(n) asm volatile("s_waitcnt vmcnt(" #n ")" ::: "memory")
; #define PG8_BAR __builtin_amdgcn_s_barrier()
;     __host__ __device__ bool next(int i, Unit& u) const {
;         u.half = 0;
;         long L = (long)i * G + c;
;         if (tail > 0) { if (i > 0) return false; const int nt = nwg - tail * G; if (nt <= 0 || 2 * nt > G || c >= 2 * nt) return false; L = (long)tail * G + (c % nt); u.half = 1 + c / nt; }
;         else if (i >= rmax) return false;
;         if (L >= nwg) return false;
;         int wgid = (int)L; { const int q = nwg / NXCD, r = nwg % NXCD, xcd = wgid % NXCD, off = wgid / NXCD; wgid = (xcd < r ? xcd * (q + 1) : r * (q + 1) + (xcd - r) * q) + off; }
;         const int nig = wgm * nN, gid = wgid / nig, fm = gid * wgm, gsz = (nM - fm) < wgm ? (nM - fm) : wgm;
;         u.pm = pm0 + fm + ((wgid % nig) % gsz); u.pn = (wgid % nig) / gsz; return true;
; template <class Epi, class Sched, bool ALIGN_EPI = false, bool SP2 = false, bool HALFM = false>
; __device__ __forceinline__ void gemm_phase(PG8_LAS unsigned char* lds, const Gemm g, const Sched& S, const Epi& E) {
;     ...
;     bf16x8 At[4][2], B0[2][2], B1[2][2];
;     const char* cA = (const char*)g.A + (size_t)cur.pm * tstepA + ((HALFM && cur.half == 2) ? 16384 : 0); const char* cB = (const char*)g.Bt + (size_t)cur.pn * tstep;
;     S.a_ready(cur);
;     if constexpr (SP2) {
;         PG8_STAGE(PG8_SB(0, 0), cB, voffB); PG8_STAGE(PG8_SB(0, 1), cB + hstep, voffB); PG8_STAGE(PG8_SA(0, 0), cA, voffA); PG8_STAGE(PG8_SA(0, 1), cA + hstepA, voffA);
;         if (wr == 1) PG8_BAR;
;         PG8_WAIT_V(2); PG8_BAR;
;         PG8_STAGE(PG8_SB(1, 0), cB + kstep, voffB); PG8_STAGE(PG8_SA(1, 0), cA + kstep, voffA); PG8_STAGE(PG8_SB(1, 1), cB + hstep + kstep, voffB);
;         PG8_WAIT_V(6); PG8_BAR;
;         PG8_STAGE(PG8_SA(1, 1), cA + kstep + hstepA, voffA);
.LBB0_1405:
	s_lshr_b32 s7, s8, 6
	s_lshr_b32 s9, s8, 8
	s_lshl_b32 s20, s7, 10
	s_add_u32 s21, s84, 0x33600000
	s_addc_u32 s22, s85, 0
	s_add_u32 s23, s84, 0x10800000
	s_addc_u32 s24, s85, 0
	s_add_i32 s0, s4, s0
	s_ashr_i32 s1, s0, 31
	s_lshr_b32 s1, s1, 25
	s_add_i32 s1, s0, s1
	s_ashr_i32 s4, s1, 7
	s_and_b32 s1, s1, 0xff80
	s_sub_i32 s0, s0, s1
	s_bfe_i32 s1, s0, 0x80000
	s_bfe_u32 s1, s1, 0x3000c
	s_add_i32 s1, s0, s1
	s_bfe_i32 s5, s1, 0x80000
	s_and_b32 s1, s1, 0xf8
	s_sub_i32 s0, s0, s1
	s_lshl_b32 s4, s4, 3
	s_sext_i32_i16 s5, s5
	s_sext_i32_i8 s0, s0
	s_add_i32 s48, s4, s0
	s_and_b32 s0, s2, 7
	s_lshl_b32 s0, s0, 3
	s_bfe_u32 s1, s2, 0x20003
	s_add_i32 s0, s0, s1
	s_lshr_b32 s1, s2, 5
	s_lshl_b32 s1, s1, 3
	s_cmp_eq_u32 s80, 0x100
	s_cselect_b32 s48, s0, s48
	s_cselect_b32 s5, s1, s5
	s_ashr_i32 s0, s5, 3
	s_lshr_b32 s6, s5, 3
	s_mul_hi_i32 s1, s0, 0x560000
	s_mul_i32 s0, s0, 0x560000
	s_add_u32 s14, s23, s0
	s_addc_u32 s15, s24, s1
	s_mov_b64 s[0:1], s[14:15]
	s_add_i32 s25, s20, 0
	v_lshlrev_b32_e32 v128, 4, v0
	s_add_i32 m0, s25, 0x10000
	v_mov_b32_e32 v129, 0
	v_lshl_add_u64 v[2:3], s[0:1], 0, v[128:129]
	global_load_lds_dwordx4 v128, s[0:1]
	s_mov_b64 s[0:1], 0x2000
	s_add_i32 m0, s25, 0x12000
	v_lshl_add_u64 v[2:3], v[2:3], 0, s[0:1]
	s_add_u32 s4, s14, 0x4000
	global_load_lds_dwordx4 v[2:3], off
	s_addc_u32 s5, s15, 0
	s_add_i32 m0, s25, 0x14000
	s_mul_i32 s11, s48, 0x560000
	s_mul_hi_i32 s10, s48, 0x560000
	global_load_lds_dwordx4 v128, s[4:5]
	s_add_i32 m0, s25, 0x16000
	s_add_u32 s16, s21, s11
	v_lshl_add_u64 v[2:3], s[4:5], 0, v[128:129]
	s_addc_u32 s17, s22, s10
	v_lshl_add_u64 v[2:3], v[2:3], 0, s[0:1]
	s_mov_b64 s[4:5], s[16:17]
	global_load_lds_dwordx4 v[2:3], off
	s_mov_b32 m0, s25
	s_add_i32 s26, s25, 0x2000
	v_lshl_add_u64 v[2:3], s[4:5], 0, v[128:129]
	global_load_lds_dwordx4 v128, s[4:5]
	s_add_u32 s4, s16, 0x4000
	v_lshl_add_u64 v[2:3], v[2:3], 0, s[0:1]
	s_mov_b32 m0, s26
	s_addc_u32 s5, s17, 0
	s_add_i32 s27, s25, 0x4000
	global_load_lds_dwordx4 v[2:3], off
	s_mov_b32 m0, s27
	v_lshl_add_u64 v[2:3], s[4:5], 0, v[128:129]
	s_add_i32 s28, s25, 0x6000
	global_load_lds_dwordx4 v128, s[4:5]
	v_lshl_add_u64 v[2:3], v[2:3], 0, s[0:1]
	s_mov_b32 m0, s28
	s_cmp_eq_u32 s9, 1
	global_load_lds_dwordx4 v[2:3], off
	s_cselect_b64 s[4:5], -1, 0
	s_cmp_lg_u32 s9, 1
	s_mov_b32 s12, 0
	s_cbranch_scc1 .LBB0_1407
	s_barrier

;     __host__ __device__ bool next(int i, Unit& u) const {
;     ...
;         if (tail > 0) { if (i > 0) return false; const int nt = nwg - tail * G; if (nt <= 0 || 2 * nt > G || c >= 2 * nt) return false; L = (long)tail * G + (c % nt); u.half = 1 + c / nt; }
;         else if (i >= rmax) return false;
;         if (L >= nwg) return false;
;         int wgid = (int)L; { const int q = nwg / NXCD, r = nwg % NXCD, xcd = wgid % NXCD, off = wgid / NXCD; wgid = (xcd < r ? xcd * (q + 1) : r * (q + 1) + (xcd - r) * q) + off; }
;         const int nig = wgm * nN, gid = wgid / nig, fm = gid * wgm, gsz = (nM - fm) < wgm ? (nM - fm) : wgm;
;         u.pm = pm0 + fm + ((wgid % nig) % gsz); u.pn = (wgid % nig) / gsz; return true;
; template <class Epi, class Sched, bool ALIGN_EPI = false, bool SP2 = false, bool HALFM = false>
; __device__ __forceinline__ void gemm_phase(PG8_LAS unsigned char* lds, const Gemm g, const Sched& S, const Epi& E) {
;     ...
;         const bool has_next = S.next(ui + 1, nxt);
;         const char* nA = has_next ? (const char*)g.A + (size_t)nxt.pm * tstepA + ((HALFM && nxt.half == 2) ? 16384 : 0) : cA; const char* nB = has_next ? (const char*)g.Bt + (size_t)nxt.pn * tstep : cB;
.LBB0_1416:
	s_ashr_i32 s0, s8, 3
	s_add_i32 s0, s10, s0
	s_ashr_i32 s1, s0, 31
	s_lshr_b32 s1, s1, 25
	s_add_i32 s1, s0, s1
	s_ashr_i32 s8, s1, 7
	s_lshl_b32 s8, s8, 3
	s_sub_i32 s9, 64, s8
	s_min_i32 s9, s9, 8
	s_abs_i32 s10, s9
	v_cvt_f32_u32_e32 v0, s10
	s_sub_i32 s13, 0, s10
	s_and_b32 s1, s1, 0xffffff80
	s_sub_i32 s0, s0, s1
	v_rcp_iflag_f32_e32 v0, v0
	s_abs_i32 s1, s0
	s_xor_b32 s11, s0, s9
	s_ashr_i32 s11, s11, 31
	v_mul_f32_e32 v0, 0x4f7ffffe, v0
	v_cvt_u32_f32_e32 v0, v0
	s_nop 0
	v_readfirstlane_b32 s18, v0
	s_mul_i32 s13, s13, s18
	s_mul_hi_u32 s13, s18, s13
	s_add_i32 s18, s18, s13
	s_mul_hi_u32 s13, s1, s18
	s_mul_i32 s18, s13, s10
	s_sub_i32 s1, s1, s18
	s_add_i32 s19, s13, 1
	s_sub_i32 s18, s1, s10
	s_cmp_ge_u32 s1, s10
	s_cselect_b32 s13, s19, s13
	s_cselect_b32 s1, s18, s1
	s_add_i32 s18, s13, 1
	s_cmp_ge_u32 s1, s10
	s_cselect_b32 s1, s18, s13
	s_xor_b32 s1, s1, s11
	s_sub_i32 s46, s1, s11
	s_mul_i32 s1, s46, s9
	s_sub_i32 s0, s0, s1
	s_add_i32 s47, s8, s0
	s_and_b32 s0, s2, 7
	s_lshl_b32 s0, s0, 3
	s_bfe_u32 s1, s2, 0x20003
	s_add_i32 s0, s0, s1
	s_lshr_b32 s1, s45, 1
	s_lshl_b32 s1, s1, 2
	s_add_i32 s0, s0, s1
	s_and_b32 s1, s45, 1
	s_lshl_b32 s1, s1, 3
	s_cmp_eq_u32 s80, 0x100
	s_cselect_b32 s47, s0, s47
	s_lshr_b32 s0, s2, 5
	s_add_i32 s1, s1, s0
	s_cmp_eq_u32 s80, 0x100
	s_cselect_b32 s46, s1, s46
	s_mov_b64 s[8:9], -1
